# counted vmcnt wait in the expert-weight conversion loop (next tile's prefetch stays in flight) + 96 workgroups convert tiles 1152..10751 during the dense gate/up GEMM phase
# speedup vs baseline: 1.0333x; 1.0181x over previous
.LBB0_377:
	v_mul_u32_u24_e32 v66, s46, v141
	v_lshlrev_b32_e32 v134, 2, v66
	v_lshl_add_u64 v[66:67], s[2:3], 0, v[134:135]
	v_mov_b32_e32 v137, v135
	v_lshl_add_u64 v[66:67], v[66:67], 0, v[136:137]
	s_lshl_b32 s8, s46, 5
	v_lshl_add_u64 v[74:75], v[66:67], 0, s[8:9]
	global_load_dwordx4 v[66:69], v[66:67], off nt
	s_nop 0
	global_load_dwordx4 v[70:73], v[74:75], off nt
	v_lshl_add_u64 v[74:75], v[74:75], 0, s[8:9]
	v_lshl_add_u64 v[82:83], v[74:75], 0, s[8:9]
	global_load_dwordx4 v[74:77], v[74:75], off nt
	s_nop 0
	global_load_dwordx4 v[78:81], v[82:83], off nt
	v_lshl_add_u64 v[82:83], v[82:83], 0, s[8:9]
	v_lshl_add_u64 v[90:91], v[82:83], 0, s[8:9]
	global_load_dwordx4 v[82:85], v[82:83], off nt
	s_nop 0
	global_load_dwordx4 v[86:89], v[90:91], off nt
	v_lshl_add_u64 v[90:91], v[90:91], 0, s[8:9]
	v_lshl_add_u64 v[98:99], v[90:91], 0, s[8:9]
	v_lshl_add_u64 v[102:103], v[98:99], 0, s[8:9]
	v_lshl_add_u64 v[106:107], v[102:103], 0, s[8:9]
	v_lshl_add_u64 v[110:111], v[106:107], 0, s[8:9]
	v_lshl_add_u64 v[114:115], v[110:111], 0, s[8:9]
	v_lshl_add_u64 v[118:119], v[114:115], 0, s[8:9]
	v_lshl_add_u64 v[122:123], v[118:119], 0, s[8:9]
	v_lshl_add_u64 v[126:127], v[122:123], 0, s[8:9]
	global_load_dwordx4 v[90:93], v[90:91], off nt
	s_nop 0
	global_load_dwordx4 v[94:97], v[98:99], off nt
	s_nop 0
	global_load_dwordx4 v[98:101], v[102:103], off nt
	s_nop 0
	global_load_dwordx4 v[102:105], v[106:107], off nt
	s_nop 0
	global_load_dwordx4 v[106:109], v[110:111], off nt
	s_nop 0
	global_load_dwordx4 v[110:113], v[114:115], off nt
	s_nop 0
	global_load_dwordx4 v[114:117], v[118:119], off nt
	s_nop 0
	global_load_dwordx4 v[118:121], v[122:123], off nt
	s_nop 0
	global_load_dwordx4 v[122:125], v[126:127], off nt
	v_lshl_add_u64 v[126:127], v[126:127], 0, s[8:9]
	global_load_dwordx4 v[126:129], v[126:127], off nt
	s_waitcnt vmcnt(16)
	s_branch .Lmoe_w1

.Lmoe_w1:
	ds_write_b128 v142, v[2:5]
	s_waitcnt lgkmcnt(1)
	ds_write_b128 v142, v[6:9] offset:8192
	ds_write_b128 v142, v[10:13] offset:16384
	ds_write_b128 v142, v[14:17] offset:24576
	ds_write_b128 v142, v[18:21] offset:32768
	ds_write_b128 v142, v[22:25] offset:40960
	ds_write_b128 v142, v[26:29] offset:49152
	ds_write_b128 v142, v[30:33] offset:57344
	ds_write_b128 v143, v[34:37]
	ds_write_b128 v144, v[38:41]
	ds_write_b128 v145, v[42:45]
	ds_write_b128 v146, v[46:49]
	ds_write_b128 v147, v[50:53]
	ds_write_b128 v148, v[54:57]
	ds_write_b128 v149, v[58:61]
	ds_write_b128 v150, v[62:65]
	s_waitcnt lgkmcnt(0)
	s_barrier
	ds_read2st64_b32 v[130:131], v151 offset1:4
	ds_read2st64_b32 v[132:133], v151 offset0:8 offset1:12
	ds_read2st64_b32 v[164:165], v151 offset0:24 offset1:28
	ds_read2st64_b32 v[166:167], v151 offset0:56 offset1:60
	s_cmp_gt_i32 s10, 1
	s_waitcnt lgkmcnt(3)
	v_mul_f32_e32 v130, 0x43000000, v130
	v_mul_f32_e32 v131, 0x43000000, v131
	s_waitcnt lgkmcnt(2)
	v_mul_f32_e32 v134, 0x43000000, v132
	v_med3_f32 v132, v130, s11, v155
	v_med3_f32 v131, v131, s11, v155
	v_mov_b32_e32 v130, v135
	v_mul_f32_e32 v137, 0x43000000, v133
	v_cvt_pk_fp8_f32 v130, v132, v131
	ds_read2st64_b32 v[132:133], v151 offset0:16 offset1:20
	v_med3_f32 v131, v134, s11, v155
	v_med3_f32 v134, v137, s11, v155
	v_cvt_pk_fp8_f32 v130, v131, v134 op_sel:[0,0,1]
	s_waitcnt lgkmcnt(2)
	v_mul_f32_e32 v134, 0x43000000, v164
	s_waitcnt lgkmcnt(0)
	v_mul_f32_e32 v131, 0x43000000, v132
	v_mul_f32_e32 v132, 0x43000000, v133
	v_med3_f32 v133, v131, s11, v155
	v_med3_f32 v132, v132, s11, v155
	v_mov_b32_e32 v131, v135
	v_cvt_pk_fp8_f32 v131, v133, v132
	ds_read2st64_b32 v[132:133], v151 offset0:32 offset1:36
	v_mul_f32_e32 v137, 0x43000000, v165
	ds_read2st64_b32 v[164:165], v151 offset0:40 offset1:44
	v_med3_f32 v134, v134, s11, v155
	v_med3_f32 v137, v137, s11, v155
	s_waitcnt lgkmcnt(1)
	v_mul_f32_e32 v132, 0x43000000, v132
	v_mul_f32_e32 v133, 0x43000000, v133
	v_cvt_pk_fp8_f32 v131, v134, v137 op_sel:[0,0,1]
	s_waitcnt lgkmcnt(0)
	v_mul_f32_e32 v134, 0x43000000, v164
	v_med3_f32 v164, v132, s11, v155
	v_med3_f32 v133, v133, s11, v155
	v_mov_b32_e32 v132, v135
	v_mul_f32_e32 v137, 0x43000000, v165
	v_cvt_pk_fp8_f32 v132, v164, v133
	ds_read2st64_b32 v[164:165], v151 offset0:48 offset1:52
	v_med3_f32 v133, v134, s11, v155
	v_med3_f32 v134, v137, s11, v155
	v_cvt_pk_fp8_f32 v132, v133, v134 op_sel:[0,0,1]
	v_mul_f32_e32 v137, 0x43000000, v166
	s_waitcnt lgkmcnt(0)
	v_mul_f32_e32 v133, 0x43000000, v164
	v_mul_f32_e32 v134, 0x43000000, v165
	v_med3_f32 v164, v133, s11, v155
	v_med3_f32 v134, v134, s11, v155
	v_mov_b32_e32 v133, v135
	v_cvt_pk_fp8_f32 v133, v164, v134
	ds_read2st64_b32 v[164:165], v151 offset0:64 offset1:68
	v_mul_f32_e32 v168, 0x43000000, v167
	ds_read2st64_b32 v[166:167], v151 offset0:72 offset1:76
	v_med3_f32 v134, v137, s11, v155
	v_med3_f32 v137, v168, s11, v155
	v_cvt_pk_fp8_f32 v133, v134, v137 op_sel:[0,0,1]
	s_waitcnt lgkmcnt(1)
	v_mul_f32_e32 v134, 0x43000000, v164
	v_mul_f32_e32 v137, 0x43000000, v165
	s_waitcnt lgkmcnt(0)
	v_mul_f32_e32 v165, 0x43000000, v166
	v_mul_f32_e32 v170, 0x43000000, v167
	v_med3_f32 v134, v134, s11, v155
	v_med3_f32 v137, v137, s11, v155
	v_mov_b32_e32 v164, v135
	ds_read2st64_b32 v[166:167], v151 offset0:80 offset1:84
	v_cvt_pk_fp8_f32 v164, v134, v137
	ds_read2st64_b32 v[168:169], v151 offset0:88 offset1:92
	v_med3_f32 v134, v165, s11, v155
	v_med3_f32 v137, v170, s11, v155
	v_cvt_pk_fp8_f32 v164, v134, v137 op_sel:[0,0,1]
	s_waitcnt lgkmcnt(1)
	v_mul_f32_e32 v134, 0x43000000, v166
	v_mul_f32_e32 v137, 0x43000000, v167
	s_waitcnt lgkmcnt(0)
	v_mul_f32_e32 v168, 0x43000000, v168
	v_med3_f32 v134, v134, s11, v155
	v_med3_f32 v137, v137, s11, v155
	v_mov_b32_e32 v165, v135
	ds_read2st64_b32 v[166:167], v151 offset0:96 offset1:100
	v_mul_f32_e32 v170, 0x43000000, v169
	v_cvt_pk_fp8_f32 v165, v134, v137
	v_med3_f32 v134, v168, s11, v155
	ds_read2st64_b32 v[168:169], v151 offset0:104 offset1:108
	v_med3_f32 v137, v170, s11, v155
	v_cvt_pk_fp8_f32 v165, v134, v137 op_sel:[0,0,1]
	s_waitcnt lgkmcnt(1)
	v_mul_f32_e32 v134, 0x43000000, v166
	v_mul_f32_e32 v137, 0x43000000, v167
	s_waitcnt lgkmcnt(0)
	v_mul_f32_e32 v167, 0x43000000, v168
	v_mul_f32_e32 v172, 0x43000000, v169
	v_med3_f32 v134, v134, s11, v155
	v_med3_f32 v137, v137, s11, v155
	v_mov_b32_e32 v166, v135
	ds_read2st64_b32 v[168:169], v151 offset0:112 offset1:116
	v_cvt_pk_fp8_f32 v166, v134, v137
	ds_read2st64_b32 v[170:171], v151 offset0:120 offset1:124
	v_med3_f32 v134, v167, s11, v155
	v_med3_f32 v137, v172, s11, v155
	v_cvt_pk_fp8_f32 v166, v134, v137 op_sel:[0,0,1]
	s_waitcnt lgkmcnt(1)
	v_mul_f32_e32 v134, 0x43000000, v168
	v_mul_f32_e32 v137, 0x43000000, v169
	s_waitcnt lgkmcnt(0)
	v_mul_f32_e32 v170, 0x43000000, v170
	v_med3_f32 v134, v134, s11, v155
	v_med3_f32 v137, v137, s11, v155
	v_mov_b32_e32 v167, v135
	ds_read2st64_b32 v[168:169], v151 offset0:128 offset1:132
	v_mul_f32_e32 v172, 0x43000000, v171
	v_cvt_pk_fp8_f32 v167, v134, v137
	v_med3_f32 v134, v170, s11, v155
	ds_read2st64_b32 v[170:171], v151 offset0:136 offset1:140
	v_med3_f32 v137, v172, s11, v155
	v_cvt_pk_fp8_f32 v167, v134, v137 op_sel:[0,0,1]
	s_waitcnt lgkmcnt(1)
	v_mul_f32_e32 v134, 0x43000000, v168
	v_mul_f32_e32 v137, 0x43000000, v169
	s_waitcnt lgkmcnt(0)
	v_mul_f32_e32 v169, 0x43000000, v170
	v_mul_f32_e32 v174, 0x43000000, v171
	v_med3_f32 v134, v134, s11, v155
	v_med3_f32 v137, v137, s11, v155
	v_mov_b32_e32 v168, v135
	ds_read2st64_b32 v[170:171], v151 offset0:144 offset1:148
	v_cvt_pk_fp8_f32 v168, v134, v137
	ds_read2st64_b32 v[172:173], v151 offset0:152 offset1:156
	v_med3_f32 v134, v169, s11, v155
	v_med3_f32 v137, v174, s11, v155
	v_cvt_pk_fp8_f32 v168, v134, v137 op_sel:[0,0,1]
	s_waitcnt lgkmcnt(1)
	v_mul_f32_e32 v134, 0x43000000, v170
	v_mul_f32_e32 v137, 0x43000000, v171
	s_waitcnt lgkmcnt(0)
	v_mul_f32_e32 v172, 0x43000000, v172
	v_med3_f32 v134, v134, s11, v155
	v_med3_f32 v137, v137, s11, v155
	v_mov_b32_e32 v169, v135
	ds_read2st64_b32 v[170:171], v151 offset0:160 offset1:164
	v_mul_f32_e32 v174, 0x43000000, v173
	v_cvt_pk_fp8_f32 v169, v134, v137
	v_med3_f32 v134, v172, s11, v155
	ds_read2st64_b32 v[172:173], v151 offset0:168 offset1:172
	v_med3_f32 v137, v174, s11, v155
	v_cvt_pk_fp8_f32 v169, v134, v137 op_sel:[0,0,1]
	s_waitcnt lgkmcnt(1)
	v_mul_f32_e32 v134, 0x43000000, v170
	v_mul_f32_e32 v137, 0x43000000, v171
	s_waitcnt lgkmcnt(0)
	v_mul_f32_e32 v171, 0x43000000, v172
	v_mul_f32_e32 v176, 0x43000000, v173
	v_med3_f32 v134, v134, s11, v155
	v_med3_f32 v137, v137, s11, v155
	v_mov_b32_e32 v170, v135
	ds_read2st64_b32 v[172:173], v151 offset0:176 offset1:180
	v_cvt_pk_fp8_f32 v170, v134, v137
	ds_read2st64_b32 v[174:175], v151 offset0:184 offset1:188
	v_med3_f32 v134, v171, s11, v155
	v_med3_f32 v137, v176, s11, v155
	v_cvt_pk_fp8_f32 v170, v134, v137 op_sel:[0,0,1]
	s_waitcnt lgkmcnt(1)
	v_mul_f32_e32 v134, 0x43000000, v172
	v_mul_f32_e32 v137, 0x43000000, v173
	s_waitcnt lgkmcnt(0)
	v_mul_f32_e32 v174, 0x43000000, v174
	v_med3_f32 v134, v134, s11, v155
	v_med3_f32 v137, v137, s11, v155
	v_mov_b32_e32 v171, v135
	ds_read2st64_b32 v[172:173], v151 offset0:192 offset1:196
	v_mul_f32_e32 v176, 0x43000000, v175
	v_cvt_pk_fp8_f32 v171, v134, v137
	v_med3_f32 v134, v174, s11, v155
	ds_read2st64_b32 v[174:175], v151 offset0:200 offset1:204
	v_med3_f32 v137, v176, s11, v155
	v_cvt_pk_fp8_f32 v171, v134, v137 op_sel:[0,0,1]
	s_waitcnt lgkmcnt(1)
	v_mul_f32_e32 v134, 0x43000000, v172
	v_mul_f32_e32 v137, 0x43000000, v173
	s_waitcnt lgkmcnt(0)
	v_mul_f32_e32 v173, 0x43000000, v174
	v_mul_f32_e32 v178, 0x43000000, v175
	v_med3_f32 v134, v134, s11, v155
	v_med3_f32 v137, v137, s11, v155
	v_mov_b32_e32 v172, v135
	ds_read2st64_b32 v[174:175], v151 offset0:208 offset1:212
	v_cvt_pk_fp8_f32 v172, v134, v137
	ds_read2st64_b32 v[176:177], v151 offset0:216 offset1:220
	v_med3_f32 v134, v173, s11, v155
	v_med3_f32 v137, v178, s11, v155
	v_cvt_pk_fp8_f32 v172, v134, v137 op_sel:[0,0,1]
	s_waitcnt lgkmcnt(1)
	v_mul_f32_e32 v134, 0x43000000, v174
	v_mul_f32_e32 v137, 0x43000000, v175
	s_waitcnt lgkmcnt(0)
	v_mul_f32_e32 v176, 0x43000000, v176
	v_med3_f32 v134, v134, s11, v155
	v_med3_f32 v137, v137, s11, v155
	v_mov_b32_e32 v173, v135
	ds_read2st64_b32 v[174:175], v151 offset0:224 offset1:228
	v_mul_f32_e32 v178, 0x43000000, v177
	v_cvt_pk_fp8_f32 v173, v134, v137
	v_med3_f32 v134, v176, s11, v155
	ds_read2st64_b32 v[176:177], v151 offset0:232 offset1:236
	v_med3_f32 v137, v178, s11, v155
	v_cvt_pk_fp8_f32 v173, v134, v137 op_sel:[0,0,1]
	s_waitcnt lgkmcnt(1)
	v_mul_f32_e32 v134, 0x43000000, v174
	v_mul_f32_e32 v137, 0x43000000, v175
	s_waitcnt lgkmcnt(0)
	v_mul_f32_e32 v175, 0x43000000, v176
	v_mul_f32_e32 v180, 0x43000000, v177
	v_med3_f32 v134, v134, s11, v155
	v_med3_f32 v137, v137, s11, v155
	v_mov_b32_e32 v174, v135
	ds_read2st64_b32 v[176:177], v151 offset0:240 offset1:244
	v_cvt_pk_fp8_f32 v174, v134, v137
	v_med3_f32 v134, v175, s11, v155
	ds_read2st64_b32 v[178:179], v151 offset0:248 offset1:252
	v_med3_f32 v137, v180, s11, v155
	v_cvt_pk_fp8_f32 v174, v134, v137 op_sel:[0,0,1]
	s_waitcnt lgkmcnt(1)
	v_mul_f32_e32 v134, 0x43000000, v176
	v_mul_f32_e32 v137, 0x43000000, v177
	v_med3_f32 v134, v134, s11, v155
	v_med3_f32 v137, v137, s11, v155
	v_mov_b32_e32 v175, v135
	v_cvt_pk_fp8_f32 v175, v134, v137
	s_waitcnt lgkmcnt(0)
	v_mul_f32_e32 v176, 0x43000000, v178
	v_mul_f32_e32 v134, 0x43000000, v179
	v_med3_f32 v137, v176, s11, v155
	v_med3_f32 v134, v134, s11, v155
	v_cvt_pk_fp8_f32 v175, v137, v134 op_sel:[0,0,1]
	s_barrier
	ds_write_b128 v156, v[130:133]
	ds_write_b128 v157, v[164:167]
	ds_write_b128 v158, v[168:171]
	ds_write_b128 v159, v[172:175]
	s_waitcnt lgkmcnt(0)
	s_barrier
	ds_read_b128 v[130:133], v160
	v_add_u32_e32 v164, s4, v140
	s_cselect_b64 s[46:47], -1, 0
	s_mov_b64 s[2:3], -1
	s_and_b64 vcc, exec, s[46:47]
	v_lshlrev_b32_e32 v165, 1, v164
	v_add_u32_e32 v137, s0, v138
	s_cbranch_vccz .LBB0_380
	v_lshlrev_b32_e32 v134, 2, v164
	v_lshrrev_b32_e32 v166, 1, v164
	v_and_b32_e32 v167, 0xffffffe3, v164
	v_and_or_b32 v168, v166, 12, v167
	v_and_or_b32 v169, v134, 16, v167
	v_ashrrev_i32_e32 v166, 7, v164
	v_ashrrev_i32_e32 v134, 7, v137
	v_mad_u64_u32 v[166:167], s[2:3], v166, 56, v[134:135]
	v_lshrrev_b32_e32 v134, 3, v169
	v_bfe_u32 v169, v137, 6, 1
	v_ashrrev_i32_e32 v167, 31, v166
	v_and_or_b32 v134, v134, 14, v169
	v_lshlrev_b32_e32 v168, 6, v168
	v_and_b32_e32 v169, 63, v137
	v_lshlrev_b64 v[166:167], 14, v[166:167]
	v_and_or_b32 v168, v168, s16, v169
	v_lshlrev_b32_e32 v134, 10, v134
	v_and_b32_e32 v169, 32, v165
	v_bitop3_b32 v134, v134, v168, v169 bitop3:0xf6
	v_lshl_add_u64 v[166:167], s[6:7], 0, v[166:167]
	v_lshl_add_u64 v[166:167], v[166:167], 0, v[134:135]
	s_waitcnt lgkmcnt(0)
	global_store_dwordx4 v[166:167], v[130:133], off nt
	s_mov_b64 s[2:3], 0

.LBB0_401:
	v_mul_u32_u24_e32 v2, s44, v141
	v_lshlrev_b32_e32 v134, 2, v2
	v_lshl_add_u64 v[2:3], s[2:3], 0, v[134:135]
	v_mov_b32_e32 v137, v135
	v_lshl_add_u64 v[2:3], v[2:3], 0, v[136:137]
	s_lshl_b32 s8, s44, 5
	v_lshl_add_u64 v[10:11], v[2:3], 0, s[8:9]
	global_load_dwordx4 v[2:5], v[2:3], off nt
	s_nop 0
	global_load_dwordx4 v[6:9], v[10:11], off nt
	v_lshl_add_u64 v[10:11], v[10:11], 0, s[8:9]
	v_lshl_add_u64 v[18:19], v[10:11], 0, s[8:9]
	global_load_dwordx4 v[10:13], v[10:11], off nt
	s_nop 0
	global_load_dwordx4 v[14:17], v[18:19], off nt
	v_lshl_add_u64 v[18:19], v[18:19], 0, s[8:9]
	v_lshl_add_u64 v[26:27], v[18:19], 0, s[8:9]
	global_load_dwordx4 v[18:21], v[18:19], off nt
	s_nop 0
	global_load_dwordx4 v[22:25], v[26:27], off nt
	v_lshl_add_u64 v[26:27], v[26:27], 0, s[8:9]
	v_lshl_add_u64 v[34:35], v[26:27], 0, s[8:9]
	v_lshl_add_u64 v[38:39], v[34:35], 0, s[8:9]
	v_lshl_add_u64 v[42:43], v[38:39], 0, s[8:9]
	v_lshl_add_u64 v[46:47], v[42:43], 0, s[8:9]
	v_lshl_add_u64 v[50:51], v[46:47], 0, s[8:9]
	v_lshl_add_u64 v[54:55], v[50:51], 0, s[8:9]
	v_lshl_add_u64 v[58:59], v[54:55], 0, s[8:9]
	v_lshl_add_u64 v[62:63], v[58:59], 0, s[8:9]
	global_load_dwordx4 v[26:29], v[26:27], off nt
	s_nop 0
	global_load_dwordx4 v[30:33], v[34:35], off nt
	s_nop 0
	global_load_dwordx4 v[34:37], v[38:39], off nt
	s_nop 0
	global_load_dwordx4 v[38:41], v[42:43], off nt
	s_nop 0
	global_load_dwordx4 v[42:45], v[46:47], off nt
	s_nop 0
	global_load_dwordx4 v[46:49], v[50:51], off nt
	s_nop 0
	global_load_dwordx4 v[50:53], v[54:55], off nt
	s_nop 0
	global_load_dwordx4 v[54:57], v[58:59], off nt
	s_nop 0
	global_load_dwordx4 v[58:61], v[62:63], off nt
	v_lshl_add_u64 v[62:63], v[62:63], 0, s[8:9]
	global_load_dwordx4 v[62:65], v[62:63], off nt
	s_waitcnt vmcnt(16)
	s_branch .Lmoe_w2
.LBB0_402:
	s_waitcnt vmcnt(0)
.Lmoe_w2:
	ds_write_b128 v142, v[66:69]
	ds_write_b128 v142, v[70:73] offset:8192
	ds_write_b128 v142, v[74:77] offset:16384
	ds_write_b128 v142, v[78:81] offset:24576
	ds_write_b128 v142, v[82:85] offset:32768
	ds_write_b128 v142, v[86:89] offset:40960
	ds_write_b128 v142, v[90:93] offset:49152
	ds_write_b128 v142, v[94:97] offset:57344
	ds_write_b128 v143, v[98:101]
	ds_write_b128 v144, v[102:105]
	ds_write_b128 v145, v[106:109]
	ds_write_b128 v146, v[110:113]
	ds_write_b128 v147, v[114:117]
	ds_write_b128 v148, v[118:121]
	ds_write_b128 v149, v[122:125]
	ds_write_b128 v150, v[126:129]
	s_waitcnt lgkmcnt(0)
	s_barrier
	ds_read2st64_b32 v[130:131], v151 offset1:4
	ds_read2st64_b32 v[132:133], v151 offset0:8 offset1:12
	ds_read2st64_b32 v[164:165], v151 offset0:24 offset1:28
	ds_read2st64_b32 v[166:167], v151 offset0:56 offset1:60
	s_cmp_gt_i32 s17, 1
	s_waitcnt lgkmcnt(3)
	v_mul_f32_e32 v130, 0x43000000, v130
	v_mul_f32_e32 v131, 0x43000000, v131
	s_waitcnt lgkmcnt(2)
	v_mul_f32_e32 v134, 0x43000000, v132
	v_med3_f32 v132, v130, s11, v155
	v_med3_f32 v131, v131, s11, v155
	v_mov_b32_e32 v130, v135
	v_mul_f32_e32 v137, 0x43000000, v133
	v_cvt_pk_fp8_f32 v130, v132, v131
	ds_read2st64_b32 v[132:133], v151 offset0:16 offset1:20
	v_med3_f32 v131, v134, s11, v155
	v_med3_f32 v134, v137, s11, v155
	v_cvt_pk_fp8_f32 v130, v131, v134 op_sel:[0,0,1]
	s_waitcnt lgkmcnt(2)
	v_mul_f32_e32 v134, 0x43000000, v164
	s_waitcnt lgkmcnt(0)
	v_mul_f32_e32 v131, 0x43000000, v132
	v_mul_f32_e32 v132, 0x43000000, v133
	v_med3_f32 v133, v131, s11, v155
	v_med3_f32 v132, v132, s11, v155
	v_mov_b32_e32 v131, v135
	v_cvt_pk_fp8_f32 v131, v133, v132
	ds_read2st64_b32 v[132:133], v151 offset0:32 offset1:36
	v_mul_f32_e32 v137, 0x43000000, v165
	ds_read2st64_b32 v[164:165], v151 offset0:40 offset1:44
	v_med3_f32 v134, v134, s11, v155
	v_med3_f32 v137, v137, s11, v155
	s_waitcnt lgkmcnt(1)
	v_mul_f32_e32 v132, 0x43000000, v132
	v_mul_f32_e32 v133, 0x43000000, v133
	v_cvt_pk_fp8_f32 v131, v134, v137 op_sel:[0,0,1]
	s_waitcnt lgkmcnt(0)
	v_mul_f32_e32 v134, 0x43000000, v164
	v_med3_f32 v164, v132, s11, v155
	v_med3_f32 v133, v133, s11, v155
	v_mov_b32_e32 v132, v135
	v_mul_f32_e32 v137, 0x43000000, v165
	v_cvt_pk_fp8_f32 v132, v164, v133
	ds_read2st64_b32 v[164:165], v151 offset0:48 offset1:52
	v_med3_f32 v133, v134, s11, v155
	v_med3_f32 v134, v137, s11, v155
	v_cvt_pk_fp8_f32 v132, v133, v134 op_sel:[0,0,1]
	v_mul_f32_e32 v137, 0x43000000, v166
	s_waitcnt lgkmcnt(0)
	v_mul_f32_e32 v133, 0x43000000, v164
	v_mul_f32_e32 v134, 0x43000000, v165
	v_med3_f32 v164, v133, s11, v155
	v_med3_f32 v134, v134, s11, v155
	v_mov_b32_e32 v133, v135
	v_cvt_pk_fp8_f32 v133, v164, v134
	ds_read2st64_b32 v[164:165], v151 offset0:64 offset1:68
	v_mul_f32_e32 v168, 0x43000000, v167
	ds_read2st64_b32 v[166:167], v151 offset0:72 offset1:76
	v_med3_f32 v134, v137, s11, v155
	v_med3_f32 v137, v168, s11, v155
	v_cvt_pk_fp8_f32 v133, v134, v137 op_sel:[0,0,1]
	s_waitcnt lgkmcnt(1)
	v_mul_f32_e32 v134, 0x43000000, v164
	v_mul_f32_e32 v137, 0x43000000, v165
	s_waitcnt lgkmcnt(0)
	v_mul_f32_e32 v165, 0x43000000, v166
	v_mul_f32_e32 v170, 0x43000000, v167
	v_med3_f32 v134, v134, s11, v155
	v_med3_f32 v137, v137, s11, v155
	v_mov_b32_e32 v164, v135
	ds_read2st64_b32 v[166:167], v151 offset0:80 offset1:84
	v_cvt_pk_fp8_f32 v164, v134, v137
	ds_read2st64_b32 v[168:169], v151 offset0:88 offset1:92
	v_med3_f32 v134, v165, s11, v155
	v_med3_f32 v137, v170, s11, v155
	v_cvt_pk_fp8_f32 v164, v134, v137 op_sel:[0,0,1]
	s_waitcnt lgkmcnt(1)
	v_mul_f32_e32 v134, 0x43000000, v166
	v_mul_f32_e32 v137, 0x43000000, v167
	s_waitcnt lgkmcnt(0)
	v_mul_f32_e32 v168, 0x43000000, v168
	v_med3_f32 v134, v134, s11, v155
	v_med3_f32 v137, v137, s11, v155
	v_mov_b32_e32 v165, v135
	ds_read2st64_b32 v[166:167], v151 offset0:96 offset1:100
	v_mul_f32_e32 v170, 0x43000000, v169
	v_cvt_pk_fp8_f32 v165, v134, v137
	v_med3_f32 v134, v168, s11, v155
	ds_read2st64_b32 v[168:169], v151 offset0:104 offset1:108
	v_med3_f32 v137, v170, s11, v155
	v_cvt_pk_fp8_f32 v165, v134, v137 op_sel:[0,0,1]
	s_waitcnt lgkmcnt(1)
	v_mul_f32_e32 v134, 0x43000000, v166
	v_mul_f32_e32 v137, 0x43000000, v167
	s_waitcnt lgkmcnt(0)
	v_mul_f32_e32 v167, 0x43000000, v168
	v_mul_f32_e32 v172, 0x43000000, v169
	v_med3_f32 v134, v134, s11, v155
	v_med3_f32 v137, v137, s11, v155
	v_mov_b32_e32 v166, v135
	ds_read2st64_b32 v[168:169], v151 offset0:112 offset1:116
	v_cvt_pk_fp8_f32 v166, v134, v137
	ds_read2st64_b32 v[170:171], v151 offset0:120 offset1:124
	v_med3_f32 v134, v167, s11, v155
	v_med3_f32 v137, v172, s11, v155
	v_cvt_pk_fp8_f32 v166, v134, v137 op_sel:[0,0,1]
	s_waitcnt lgkmcnt(1)
	v_mul_f32_e32 v134, 0x43000000, v168
	v_mul_f32_e32 v137, 0x43000000, v169
	s_waitcnt lgkmcnt(0)
	v_mul_f32_e32 v170, 0x43000000, v170
	v_med3_f32 v134, v134, s11, v155
	v_med3_f32 v137, v137, s11, v155
	v_mov_b32_e32 v167, v135
	ds_read2st64_b32 v[168:169], v151 offset0:128 offset1:132
	v_mul_f32_e32 v172, 0x43000000, v171
	v_cvt_pk_fp8_f32 v167, v134, v137
	v_med3_f32 v134, v170, s11, v155
	ds_read2st64_b32 v[170:171], v151 offset0:136 offset1:140
	v_med3_f32 v137, v172, s11, v155
	v_cvt_pk_fp8_f32 v167, v134, v137 op_sel:[0,0,1]
	s_waitcnt lgkmcnt(1)
	v_mul_f32_e32 v134, 0x43000000, v168
	v_mul_f32_e32 v137, 0x43000000, v169
	s_waitcnt lgkmcnt(0)
	v_mul_f32_e32 v169, 0x43000000, v170
	v_mul_f32_e32 v174, 0x43000000, v171
	v_med3_f32 v134, v134, s11, v155
	v_med3_f32 v137, v137, s11, v155
	v_mov_b32_e32 v168, v135
	ds_read2st64_b32 v[170:171], v151 offset0:144 offset1:148
	v_cvt_pk_fp8_f32 v168, v134, v137
	ds_read2st64_b32 v[172:173], v151 offset0:152 offset1:156
	v_med3_f32 v134, v169, s11, v155
	v_med3_f32 v137, v174, s11, v155
	v_cvt_pk_fp8_f32 v168, v134, v137 op_sel:[0,0,1]
	s_waitcnt lgkmcnt(1)
	v_mul_f32_e32 v134, 0x43000000, v170
	v_mul_f32_e32 v137, 0x43000000, v171
	s_waitcnt lgkmcnt(0)
	v_mul_f32_e32 v172, 0x43000000, v172
	v_med3_f32 v134, v134, s11, v155
	v_med3_f32 v137, v137, s11, v155
	v_mov_b32_e32 v169, v135
	ds_read2st64_b32 v[170:171], v151 offset0:160 offset1:164
	v_mul_f32_e32 v174, 0x43000000, v173
	v_cvt_pk_fp8_f32 v169, v134, v137
	v_med3_f32 v134, v172, s11, v155
	ds_read2st64_b32 v[172:173], v151 offset0:168 offset1:172
	v_med3_f32 v137, v174, s11, v155
	v_cvt_pk_fp8_f32 v169, v134, v137 op_sel:[0,0,1]
	s_waitcnt lgkmcnt(1)
	v_mul_f32_e32 v134, 0x43000000, v170
	v_mul_f32_e32 v137, 0x43000000, v171
	s_waitcnt lgkmcnt(0)
	v_mul_f32_e32 v171, 0x43000000, v172
	v_mul_f32_e32 v176, 0x43000000, v173
	v_med3_f32 v134, v134, s11, v155
	v_med3_f32 v137, v137, s11, v155
	v_mov_b32_e32 v170, v135
	ds_read2st64_b32 v[172:173], v151 offset0:176 offset1:180
	v_cvt_pk_fp8_f32 v170, v134, v137
	ds_read2st64_b32 v[174:175], v151 offset0:184 offset1:188
	v_med3_f32 v134, v171, s11, v155
	v_med3_f32 v137, v176, s11, v155
	v_cvt_pk_fp8_f32 v170, v134, v137 op_sel:[0,0,1]
	s_waitcnt lgkmcnt(1)
	v_mul_f32_e32 v134, 0x43000000, v172
	v_mul_f32_e32 v137, 0x43000000, v173
	s_waitcnt lgkmcnt(0)
	v_mul_f32_e32 v174, 0x43000000, v174
	v_med3_f32 v134, v134, s11, v155
	v_med3_f32 v137, v137, s11, v155
	v_mov_b32_e32 v171, v135
	ds_read2st64_b32 v[172:173], v151 offset0:192 offset1:196
	v_mul_f32_e32 v176, 0x43000000, v175
	v_cvt_pk_fp8_f32 v171, v134, v137
	v_med3_f32 v134, v174, s11, v155
	ds_read2st64_b32 v[174:175], v151 offset0:200 offset1:204
	v_med3_f32 v137, v176, s11, v155
	v_cvt_pk_fp8_f32 v171, v134, v137 op_sel:[0,0,1]
	s_waitcnt lgkmcnt(1)
	v_mul_f32_e32 v134, 0x43000000, v172
	v_mul_f32_e32 v137, 0x43000000, v173
	s_waitcnt lgkmcnt(0)
	v_mul_f32_e32 v173, 0x43000000, v174
	v_mul_f32_e32 v178, 0x43000000, v175
	v_med3_f32 v134, v134, s11, v155
	v_med3_f32 v137, v137, s11, v155
	v_mov_b32_e32 v172, v135
	ds_read2st64_b32 v[174:175], v151 offset0:208 offset1:212
	v_cvt_pk_fp8_f32 v172, v134, v137
	ds_read2st64_b32 v[176:177], v151 offset0:216 offset1:220
	v_med3_f32 v134, v173, s11, v155
	v_med3_f32 v137, v178, s11, v155
	v_cvt_pk_fp8_f32 v172, v134, v137 op_sel:[0,0,1]
	s_waitcnt lgkmcnt(1)
	v_mul_f32_e32 v134, 0x43000000, v174
	v_mul_f32_e32 v137, 0x43000000, v175
	s_waitcnt lgkmcnt(0)
	v_mul_f32_e32 v176, 0x43000000, v176
	v_med3_f32 v134, v134, s11, v155
	v_med3_f32 v137, v137, s11, v155
	v_mov_b32_e32 v173, v135
	ds_read2st64_b32 v[174:175], v151 offset0:224 offset1:228
	v_mul_f32_e32 v178, 0x43000000, v177
	v_cvt_pk_fp8_f32 v173, v134, v137
	v_med3_f32 v134, v176, s11, v155
	ds_read2st64_b32 v[176:177], v151 offset0:232 offset1:236
	v_med3_f32 v137, v178, s11, v155
	v_cvt_pk_fp8_f32 v173, v134, v137 op_sel:[0,0,1]
	s_waitcnt lgkmcnt(1)
	v_mul_f32_e32 v134, 0x43000000, v174
	v_mul_f32_e32 v137, 0x43000000, v175
	s_waitcnt lgkmcnt(0)
	v_mul_f32_e32 v175, 0x43000000, v176
	v_mul_f32_e32 v180, 0x43000000, v177
	v_med3_f32 v134, v134, s11, v155
	v_med3_f32 v137, v137, s11, v155
	v_mov_b32_e32 v174, v135
	ds_read2st64_b32 v[176:177], v151 offset0:240 offset1:244
	v_cvt_pk_fp8_f32 v174, v134, v137
	v_med3_f32 v134, v175, s11, v155
	ds_read2st64_b32 v[178:179], v151 offset0:248 offset1:252
	v_med3_f32 v137, v180, s11, v155
	v_cvt_pk_fp8_f32 v174, v134, v137 op_sel:[0,0,1]
	s_waitcnt lgkmcnt(1)
	v_mul_f32_e32 v134, 0x43000000, v176
	v_mul_f32_e32 v137, 0x43000000, v177
	v_med3_f32 v134, v134, s11, v155
	v_med3_f32 v137, v137, s11, v155
	v_mov_b32_e32 v175, v135
	v_cvt_pk_fp8_f32 v175, v134, v137
	s_waitcnt lgkmcnt(0)
	v_mul_f32_e32 v176, 0x43000000, v178
	v_mul_f32_e32 v134, 0x43000000, v179
	v_med3_f32 v137, v176, s11, v155
	v_med3_f32 v134, v134, s11, v155
	v_cvt_pk_fp8_f32 v175, v137, v134 op_sel:[0,0,1]
	s_barrier
	ds_write_b128 v156, v[130:133]
	ds_write_b128 v157, v[164:167]
	ds_write_b128 v158, v[168:171]
	ds_write_b128 v159, v[172:175]
	s_waitcnt lgkmcnt(0)
	s_barrier
	ds_read_b128 v[130:133], v160
	v_add_u32_e32 v164, s36, v140
	s_cselect_b64 s[44:45], -1, 0
	s_mov_b64 s[2:3], -1
	s_and_b64 vcc, exec, s[44:45]
	v_lshlrev_b32_e32 v165, 1, v164
	v_add_u32_e32 v137, s14, v138
	s_cbranch_vccz .LBB0_404
	v_lshlrev_b32_e32 v134, 2, v164
	v_lshrrev_b32_e32 v166, 1, v164
	v_and_b32_e32 v167, 0xffffffe3, v164
	v_and_or_b32 v168, v166, 12, v167
	v_and_or_b32 v169, v134, 16, v167
	v_ashrrev_i32_e32 v166, 7, v164
	v_ashrrev_i32_e32 v134, 7, v137
	v_mad_u64_u32 v[166:167], s[2:3], v166, 56, v[134:135]
	v_lshrrev_b32_e32 v134, 3, v169
	v_bfe_u32 v169, v137, 6, 1
	v_ashrrev_i32_e32 v167, 31, v166
	v_and_or_b32 v134, v134, 14, v169
	v_lshlrev_b32_e32 v168, 6, v168
	v_and_b32_e32 v169, 63, v137
	v_lshlrev_b64 v[166:167], 14, v[166:167]
	v_and_or_b32 v168, v168, s16, v169
	v_lshlrev_b32_e32 v134, 10, v134
	v_and_b32_e32 v169, 32, v165
	v_bitop3_b32 v134, v134, v168, v169 bitop3:0xf6
	v_lshl_add_u64 v[166:167], s[40:41], 0, v[166:167]
	v_lshl_add_u64 v[166:167], v[166:167], 0, v[134:135]
	s_waitcnt lgkmcnt(0)
	global_store_dwordx4 v[166:167], v[130:133], off nt
	s_mov_b64 s[2:3], 0

.Lcv_moe_w1:
	ds_write_b128 v142, v[2:5]
	s_waitcnt lgkmcnt(1)
	ds_write_b128 v142, v[6:9] offset:8192
	ds_write_b128 v142, v[10:13] offset:16384
	ds_write_b128 v142, v[14:17] offset:24576
	ds_write_b128 v142, v[18:21] offset:32768
	ds_write_b128 v142, v[22:25] offset:40960
	ds_write_b128 v142, v[26:29] offset:49152
	ds_write_b128 v142, v[30:33] offset:57344
	ds_write_b128 v143, v[34:37]
	ds_write_b128 v144, v[38:41]
	ds_write_b128 v145, v[42:45]
	ds_write_b128 v146, v[46:49]
	ds_write_b128 v147, v[50:53]
	ds_write_b128 v148, v[54:57]
	ds_write_b128 v149, v[58:61]
	ds_write_b128 v150, v[62:65]
	s_waitcnt lgkmcnt(0)
	s_barrier
	ds_read2st64_b32 v[130:131], v151 offset1:4
	ds_read2st64_b32 v[132:133], v151 offset0:8 offset1:12
	ds_read2st64_b32 v[164:165], v151 offset0:24 offset1:28
	ds_read2st64_b32 v[166:167], v151 offset0:56 offset1:60
	s_cmp_gt_i32 s10, 1
	s_waitcnt lgkmcnt(3)
	v_mul_f32_e32 v130, 0x43000000, v130
	v_mul_f32_e32 v131, 0x43000000, v131
	s_waitcnt lgkmcnt(2)
	v_mul_f32_e32 v134, 0x43000000, v132
	v_med3_f32 v132, v130, s11, v155
	v_med3_f32 v131, v131, s11, v155
	v_mov_b32_e32 v130, v135
	v_mul_f32_e32 v137, 0x43000000, v133
	v_cvt_pk_fp8_f32 v130, v132, v131
	ds_read2st64_b32 v[132:133], v151 offset0:16 offset1:20
	v_med3_f32 v131, v134, s11, v155
	v_med3_f32 v134, v137, s11, v155
	v_cvt_pk_fp8_f32 v130, v131, v134 op_sel:[0,0,1]
	s_waitcnt lgkmcnt(2)
	v_mul_f32_e32 v134, 0x43000000, v164
	s_waitcnt lgkmcnt(0)
	v_mul_f32_e32 v131, 0x43000000, v132
	v_mul_f32_e32 v132, 0x43000000, v133
	v_med3_f32 v133, v131, s11, v155
	v_med3_f32 v132, v132, s11, v155
	v_mov_b32_e32 v131, v135
	v_cvt_pk_fp8_f32 v131, v133, v132
	ds_read2st64_b32 v[132:133], v151 offset0:32 offset1:36
	v_mul_f32_e32 v137, 0x43000000, v165
	ds_read2st64_b32 v[164:165], v151 offset0:40 offset1:44
	v_med3_f32 v134, v134, s11, v155
	v_med3_f32 v137, v137, s11, v155
	s_waitcnt lgkmcnt(1)
	v_mul_f32_e32 v132, 0x43000000, v132
	v_mul_f32_e32 v133, 0x43000000, v133
	v_cvt_pk_fp8_f32 v131, v134, v137 op_sel:[0,0,1]
	s_waitcnt lgkmcnt(0)
	v_mul_f32_e32 v134, 0x43000000, v164
	v_med3_f32 v164, v132, s11, v155
	v_med3_f32 v133, v133, s11, v155
	v_mov_b32_e32 v132, v135
	v_mul_f32_e32 v137, 0x43000000, v165
	v_cvt_pk_fp8_f32 v132, v164, v133
	ds_read2st64_b32 v[164:165], v151 offset0:48 offset1:52
	v_med3_f32 v133, v134, s11, v155
	v_med3_f32 v134, v137, s11, v155
	v_cvt_pk_fp8_f32 v132, v133, v134 op_sel:[0,0,1]
	v_mul_f32_e32 v137, 0x43000000, v166
	s_waitcnt lgkmcnt(0)
	v_mul_f32_e32 v133, 0x43000000, v164
	v_mul_f32_e32 v134, 0x43000000, v165
	v_med3_f32 v164, v133, s11, v155
	v_med3_f32 v134, v134, s11, v155
	v_mov_b32_e32 v133, v135
	v_cvt_pk_fp8_f32 v133, v164, v134
	ds_read2st64_b32 v[164:165], v151 offset0:64 offset1:68
	v_mul_f32_e32 v168, 0x43000000, v167
	ds_read2st64_b32 v[166:167], v151 offset0:72 offset1:76
	v_med3_f32 v134, v137, s11, v155
	v_med3_f32 v137, v168, s11, v155
	v_cvt_pk_fp8_f32 v133, v134, v137 op_sel:[0,0,1]
	s_waitcnt lgkmcnt(1)
	v_mul_f32_e32 v134, 0x43000000, v164
	v_mul_f32_e32 v137, 0x43000000, v165
	s_waitcnt lgkmcnt(0)
	v_mul_f32_e32 v165, 0x43000000, v166
	v_mul_f32_e32 v170, 0x43000000, v167
	v_med3_f32 v134, v134, s11, v155
	v_med3_f32 v137, v137, s11, v155
	v_mov_b32_e32 v164, v135
	ds_read2st64_b32 v[166:167], v151 offset0:80 offset1:84
	v_cvt_pk_fp8_f32 v164, v134, v137
	ds_read2st64_b32 v[168:169], v151 offset0:88 offset1:92
	v_med3_f32 v134, v165, s11, v155
	v_med3_f32 v137, v170, s11, v155
	v_cvt_pk_fp8_f32 v164, v134, v137 op_sel:[0,0,1]
	s_waitcnt lgkmcnt(1)
	v_mul_f32_e32 v134, 0x43000000, v166
	v_mul_f32_e32 v137, 0x43000000, v167
	s_waitcnt lgkmcnt(0)
	v_mul_f32_e32 v168, 0x43000000, v168
	v_med3_f32 v134, v134, s11, v155
	v_med3_f32 v137, v137, s11, v155
	v_mov_b32_e32 v165, v135
	ds_read2st64_b32 v[166:167], v151 offset0:96 offset1:100
	v_mul_f32_e32 v170, 0x43000000, v169
	v_cvt_pk_fp8_f32 v165, v134, v137
	v_med3_f32 v134, v168, s11, v155
	ds_read2st64_b32 v[168:169], v151 offset0:104 offset1:108
	v_med3_f32 v137, v170, s11, v155
	v_cvt_pk_fp8_f32 v165, v134, v137 op_sel:[0,0,1]
	s_waitcnt lgkmcnt(1)
	v_mul_f32_e32 v134, 0x43000000, v166
	v_mul_f32_e32 v137, 0x43000000, v167
	s_waitcnt lgkmcnt(0)
	v_mul_f32_e32 v167, 0x43000000, v168
	v_mul_f32_e32 v172, 0x43000000, v169
	v_med3_f32 v134, v134, s11, v155
	v_med3_f32 v137, v137, s11, v155
	v_mov_b32_e32 v166, v135
	ds_read2st64_b32 v[168:169], v151 offset0:112 offset1:116
	v_cvt_pk_fp8_f32 v166, v134, v137
	ds_read2st64_b32 v[170:171], v151 offset0:120 offset1:124
	v_med3_f32 v134, v167, s11, v155
	v_med3_f32 v137, v172, s11, v155
	v_cvt_pk_fp8_f32 v166, v134, v137 op_sel:[0,0,1]
	s_waitcnt lgkmcnt(1)
	v_mul_f32_e32 v134, 0x43000000, v168
	v_mul_f32_e32 v137, 0x43000000, v169
	s_waitcnt lgkmcnt(0)
	v_mul_f32_e32 v170, 0x43000000, v170
	v_med3_f32 v134, v134, s11, v155
	v_med3_f32 v137, v137, s11, v155
	v_mov_b32_e32 v167, v135
	ds_read2st64_b32 v[168:169], v151 offset0:128 offset1:132
	v_mul_f32_e32 v172, 0x43000000, v171
	v_cvt_pk_fp8_f32 v167, v134, v137
	v_med3_f32 v134, v170, s11, v155
	ds_read2st64_b32 v[170:171], v151 offset0:136 offset1:140
	v_med3_f32 v137, v172, s11, v155
	v_cvt_pk_fp8_f32 v167, v134, v137 op_sel:[0,0,1]
	s_waitcnt lgkmcnt(1)
	v_mul_f32_e32 v134, 0x43000000, v168
	v_mul_f32_e32 v137, 0x43000000, v169
	s_waitcnt lgkmcnt(0)
	v_mul_f32_e32 v169, 0x43000000, v170
	v_mul_f32_e32 v174, 0x43000000, v171
	v_med3_f32 v134, v134, s11, v155
	v_med3_f32 v137, v137, s11, v155
	v_mov_b32_e32 v168, v135
	ds_read2st64_b32 v[170:171], v151 offset0:144 offset1:148
	v_cvt_pk_fp8_f32 v168, v134, v137
	ds_read2st64_b32 v[172:173], v151 offset0:152 offset1:156
	v_med3_f32 v134, v169, s11, v155
	v_med3_f32 v137, v174, s11, v155
	v_cvt_pk_fp8_f32 v168, v134, v137 op_sel:[0,0,1]
	s_waitcnt lgkmcnt(1)
	v_mul_f32_e32 v134, 0x43000000, v170
	v_mul_f32_e32 v137, 0x43000000, v171
	s_waitcnt lgkmcnt(0)
	v_mul_f32_e32 v172, 0x43000000, v172
	v_med3_f32 v134, v134, s11, v155
	v_med3_f32 v137, v137, s11, v155
	v_mov_b32_e32 v169, v135
	ds_read2st64_b32 v[170:171], v151 offset0:160 offset1:164
	v_mul_f32_e32 v174, 0x43000000, v173
	v_cvt_pk_fp8_f32 v169, v134, v137
	v_med3_f32 v134, v172, s11, v155
	ds_read2st64_b32 v[172:173], v151 offset0:168 offset1:172
	v_med3_f32 v137, v174, s11, v155
	v_cvt_pk_fp8_f32 v169, v134, v137 op_sel:[0,0,1]
	s_waitcnt lgkmcnt(1)
	v_mul_f32_e32 v134, 0x43000000, v170
	v_mul_f32_e32 v137, 0x43000000, v171
	s_waitcnt lgkmcnt(0)
	v_mul_f32_e32 v171, 0x43000000, v172
	v_mul_f32_e32 v176, 0x43000000, v173
	v_med3_f32 v134, v134, s11, v155
	v_med3_f32 v137, v137, s11, v155
	v_mov_b32_e32 v170, v135
	ds_read2st64_b32 v[172:173], v151 offset0:176 offset1:180
	v_cvt_pk_fp8_f32 v170, v134, v137
	ds_read2st64_b32 v[174:175], v151 offset0:184 offset1:188
	v_med3_f32 v134, v171, s11, v155
	v_med3_f32 v137, v176, s11, v155
	v_cvt_pk_fp8_f32 v170, v134, v137 op_sel:[0,0,1]
	s_waitcnt lgkmcnt(1)
	v_mul_f32_e32 v134, 0x43000000, v172
	v_mul_f32_e32 v137, 0x43000000, v173
	s_waitcnt lgkmcnt(0)
	v_mul_f32_e32 v174, 0x43000000, v174
	v_med3_f32 v134, v134, s11, v155
	v_med3_f32 v137, v137, s11, v155
	v_mov_b32_e32 v171, v135
	ds_read2st64_b32 v[172:173], v151 offset0:192 offset1:196
	v_mul_f32_e32 v176, 0x43000000, v175
	v_cvt_pk_fp8_f32 v171, v134, v137
	v_med3_f32 v134, v174, s11, v155
	ds_read2st64_b32 v[174:175], v151 offset0:200 offset1:204
	v_med3_f32 v137, v176, s11, v155
	v_cvt_pk_fp8_f32 v171, v134, v137 op_sel:[0,0,1]
	s_waitcnt lgkmcnt(1)
	v_mul_f32_e32 v134, 0x43000000, v172
	v_mul_f32_e32 v137, 0x43000000, v173
	s_waitcnt lgkmcnt(0)
	v_mul_f32_e32 v173, 0x43000000, v174
	v_mul_f32_e32 v178, 0x43000000, v175
	v_med3_f32 v134, v134, s11, v155
	v_med3_f32 v137, v137, s11, v155
	v_mov_b32_e32 v172, v135
	ds_read2st64_b32 v[174:175], v151 offset0:208 offset1:212
	v_cvt_pk_fp8_f32 v172, v134, v137
	ds_read2st64_b32 v[176:177], v151 offset0:216 offset1:220
	v_med3_f32 v134, v173, s11, v155
	v_med3_f32 v137, v178, s11, v155
	v_cvt_pk_fp8_f32 v172, v134, v137 op_sel:[0,0,1]
	s_waitcnt lgkmcnt(1)
	v_mul_f32_e32 v134, 0x43000000, v174
	v_mul_f32_e32 v137, 0x43000000, v175
	s_waitcnt lgkmcnt(0)
	v_mul_f32_e32 v176, 0x43000000, v176
	v_med3_f32 v134, v134, s11, v155
	v_med3_f32 v137, v137, s11, v155
	v_mov_b32_e32 v173, v135
	ds_read2st64_b32 v[174:175], v151 offset0:224 offset1:228
	v_mul_f32_e32 v178, 0x43000000, v177
	v_cvt_pk_fp8_f32 v173, v134, v137
	v_med3_f32 v134, v176, s11, v155
	ds_read2st64_b32 v[176:177], v151 offset0:232 offset1:236
	v_med3_f32 v137, v178, s11, v155
	v_cvt_pk_fp8_f32 v173, v134, v137 op_sel:[0,0,1]
	s_waitcnt lgkmcnt(1)
	v_mul_f32_e32 v134, 0x43000000, v174
	v_mul_f32_e32 v137, 0x43000000, v175
	s_waitcnt lgkmcnt(0)
	v_mul_f32_e32 v175, 0x43000000, v176
	v_mul_f32_e32 v180, 0x43000000, v177
	v_med3_f32 v134, v134, s11, v155
	v_med3_f32 v137, v137, s11, v155
	v_mov_b32_e32 v174, v135
	ds_read2st64_b32 v[176:177], v151 offset0:240 offset1:244
	v_cvt_pk_fp8_f32 v174, v134, v137
	v_med3_f32 v134, v175, s11, v155
	ds_read2st64_b32 v[178:179], v151 offset0:248 offset1:252
	v_med3_f32 v137, v180, s11, v155
	v_cvt_pk_fp8_f32 v174, v134, v137 op_sel:[0,0,1]
	s_waitcnt lgkmcnt(1)
	v_mul_f32_e32 v134, 0x43000000, v176
	v_mul_f32_e32 v137, 0x43000000, v177
	v_med3_f32 v134, v134, s11, v155
	v_med3_f32 v137, v137, s11, v155
	v_mov_b32_e32 v175, v135
	v_cvt_pk_fp8_f32 v175, v134, v137
	s_waitcnt lgkmcnt(0)
	v_mul_f32_e32 v176, 0x43000000, v178
	v_mul_f32_e32 v134, 0x43000000, v179
	v_med3_f32 v137, v176, s11, v155
	v_med3_f32 v134, v134, s11, v155
	v_cvt_pk_fp8_f32 v175, v137, v134 op_sel:[0,0,1]
	s_barrier
	ds_write_b128 v156, v[130:133]
	ds_write_b128 v157, v[164:167]
	ds_write_b128 v158, v[168:171]
	ds_write_b128 v159, v[172:175]
	s_waitcnt lgkmcnt(0)
	s_barrier
	ds_read_b128 v[130:133], v160
	v_add_u32_e32 v164, s4, v140
	s_cselect_b64 s[46:47], -1, 0
	s_mov_b64 s[2:3], -1
	s_and_b64 vcc, exec, s[46:47]
	v_lshlrev_b32_e32 v165, 1, v164
	v_add_u32_e32 v137, s0, v138
	s_cbranch_vccz .Lcv_380
	v_lshlrev_b32_e32 v134, 2, v164
	v_lshrrev_b32_e32 v166, 1, v164
	v_and_b32_e32 v167, 0xffffffe3, v164
	v_and_or_b32 v168, v166, 12, v167
	v_and_or_b32 v169, v134, 16, v167
	v_ashrrev_i32_e32 v166, 7, v164
	v_ashrrev_i32_e32 v134, 7, v137
	v_mad_u64_u32 v[166:167], s[2:3], v166, 56, v[134:135]
	v_lshrrev_b32_e32 v134, 3, v169
	v_bfe_u32 v169, v137, 6, 1
	v_ashrrev_i32_e32 v167, 31, v166
	v_and_or_b32 v134, v134, 14, v169
	v_lshlrev_b32_e32 v168, 6, v168
	v_and_b32_e32 v169, 63, v137
	v_lshlrev_b64 v[166:167], 14, v[166:167]
	v_and_or_b32 v168, v168, s68, v169
	v_lshlrev_b32_e32 v134, 10, v134
	v_and_b32_e32 v169, 32, v165
	v_bitop3_b32 v134, v134, v168, v169 bitop3:0xf6
	v_lshl_add_u64 v[166:167], s[6:7], 0, v[166:167]
	v_lshl_add_u64 v[166:167], v[166:167], 0, v[134:135]
	s_waitcnt lgkmcnt(0)
	global_store_dwordx4 v[166:167], v[130:133], off nt
	s_mov_b64 s[2:3], 0

.Lcv_402:
	s_waitcnt vmcnt(0)
.Lcv_moe_w2:
	ds_write_b128 v142, v[66:69]
	ds_write_b128 v142, v[70:73] offset:8192
	ds_write_b128 v142, v[74:77] offset:16384
	ds_write_b128 v142, v[78:81] offset:24576
	ds_write_b128 v142, v[82:85] offset:32768
	ds_write_b128 v142, v[86:89] offset:40960
	ds_write_b128 v142, v[90:93] offset:49152
	ds_write_b128 v142, v[94:97] offset:57344
	ds_write_b128 v143, v[98:101]
	ds_write_b128 v144, v[102:105]
	ds_write_b128 v145, v[106:109]
	ds_write_b128 v146, v[110:113]
	ds_write_b128 v147, v[114:117]
	ds_write_b128 v148, v[118:121]
	ds_write_b128 v149, v[122:125]
	ds_write_b128 v150, v[126:129]
	s_waitcnt lgkmcnt(0)
	s_barrier
	ds_read2st64_b32 v[130:131], v151 offset1:4
	ds_read2st64_b32 v[132:133], v151 offset0:8 offset1:12
	ds_read2st64_b32 v[164:165], v151 offset0:24 offset1:28
	ds_read2st64_b32 v[166:167], v151 offset0:56 offset1:60
	s_cmp_gt_i32 s69, 1
	s_waitcnt lgkmcnt(3)
	v_mul_f32_e32 v130, 0x43000000, v130
	v_mul_f32_e32 v131, 0x43000000, v131
	s_waitcnt lgkmcnt(2)
	v_mul_f32_e32 v134, 0x43000000, v132
	v_med3_f32 v132, v130, s11, v155
	v_med3_f32 v131, v131, s11, v155
	v_mov_b32_e32 v130, v135
	v_mul_f32_e32 v137, 0x43000000, v133
	v_cvt_pk_fp8_f32 v130, v132, v131
	ds_read2st64_b32 v[132:133], v151 offset0:16 offset1:20
	v_med3_f32 v131, v134, s11, v155
	v_med3_f32 v134, v137, s11, v155
	v_cvt_pk_fp8_f32 v130, v131, v134 op_sel:[0,0,1]
	s_waitcnt lgkmcnt(2)
	v_mul_f32_e32 v134, 0x43000000, v164
	s_waitcnt lgkmcnt(0)
	v_mul_f32_e32 v131, 0x43000000, v132
	v_mul_f32_e32 v132, 0x43000000, v133
	v_med3_f32 v133, v131, s11, v155
	v_med3_f32 v132, v132, s11, v155
	v_mov_b32_e32 v131, v135
	v_cvt_pk_fp8_f32 v131, v133, v132
	ds_read2st64_b32 v[132:133], v151 offset0:32 offset1:36
	v_mul_f32_e32 v137, 0x43000000, v165
	ds_read2st64_b32 v[164:165], v151 offset0:40 offset1:44
	v_med3_f32 v134, v134, s11, v155
	v_med3_f32 v137, v137, s11, v155
	s_waitcnt lgkmcnt(1)
	v_mul_f32_e32 v132, 0x43000000, v132
	v_mul_f32_e32 v133, 0x43000000, v133
	v_cvt_pk_fp8_f32 v131, v134, v137 op_sel:[0,0,1]
	s_waitcnt lgkmcnt(0)
	v_mul_f32_e32 v134, 0x43000000, v164
	v_med3_f32 v164, v132, s11, v155
	v_med3_f32 v133, v133, s11, v155
	v_mov_b32_e32 v132, v135
	v_mul_f32_e32 v137, 0x43000000, v165
	v_cvt_pk_fp8_f32 v132, v164, v133
	ds_read2st64_b32 v[164:165], v151 offset0:48 offset1:52
	v_med3_f32 v133, v134, s11, v155
	v_med3_f32 v134, v137, s11, v155
	v_cvt_pk_fp8_f32 v132, v133, v134 op_sel:[0,0,1]
	v_mul_f32_e32 v137, 0x43000000, v166
	s_waitcnt lgkmcnt(0)
	v_mul_f32_e32 v133, 0x43000000, v164
	v_mul_f32_e32 v134, 0x43000000, v165
	v_med3_f32 v164, v133, s11, v155
	v_med3_f32 v134, v134, s11, v155
	v_mov_b32_e32 v133, v135
	v_cvt_pk_fp8_f32 v133, v164, v134
	ds_read2st64_b32 v[164:165], v151 offset0:64 offset1:68
	v_mul_f32_e32 v168, 0x43000000, v167
	ds_read2st64_b32 v[166:167], v151 offset0:72 offset1:76
	v_med3_f32 v134, v137, s11, v155
	v_med3_f32 v137, v168, s11, v155
	v_cvt_pk_fp8_f32 v133, v134, v137 op_sel:[0,0,1]
	s_waitcnt lgkmcnt(1)
	v_mul_f32_e32 v134, 0x43000000, v164
	v_mul_f32_e32 v137, 0x43000000, v165
	s_waitcnt lgkmcnt(0)
	v_mul_f32_e32 v165, 0x43000000, v166
	v_mul_f32_e32 v170, 0x43000000, v167
	v_med3_f32 v134, v134, s11, v155
	v_med3_f32 v137, v137, s11, v155
	v_mov_b32_e32 v164, v135
	ds_read2st64_b32 v[166:167], v151 offset0:80 offset1:84
	v_cvt_pk_fp8_f32 v164, v134, v137
	ds_read2st64_b32 v[168:169], v151 offset0:88 offset1:92
	v_med3_f32 v134, v165, s11, v155
	v_med3_f32 v137, v170, s11, v155
	v_cvt_pk_fp8_f32 v164, v134, v137 op_sel:[0,0,1]
	s_waitcnt lgkmcnt(1)
	v_mul_f32_e32 v134, 0x43000000, v166
	v_mul_f32_e32 v137, 0x43000000, v167
	s_waitcnt lgkmcnt(0)
	v_mul_f32_e32 v168, 0x43000000, v168
	v_med3_f32 v134, v134, s11, v155
	v_med3_f32 v137, v137, s11, v155
	v_mov_b32_e32 v165, v135
	ds_read2st64_b32 v[166:167], v151 offset0:96 offset1:100
	v_mul_f32_e32 v170, 0x43000000, v169
	v_cvt_pk_fp8_f32 v165, v134, v137
	v_med3_f32 v134, v168, s11, v155
	ds_read2st64_b32 v[168:169], v151 offset0:104 offset1:108
	v_med3_f32 v137, v170, s11, v155
	v_cvt_pk_fp8_f32 v165, v134, v137 op_sel:[0,0,1]
	s_waitcnt lgkmcnt(1)
	v_mul_f32_e32 v134, 0x43000000, v166
	v_mul_f32_e32 v137, 0x43000000, v167
	s_waitcnt lgkmcnt(0)
	v_mul_f32_e32 v167, 0x43000000, v168
	v_mul_f32_e32 v172, 0x43000000, v169
	v_med3_f32 v134, v134, s11, v155
	v_med3_f32 v137, v137, s11, v155
	v_mov_b32_e32 v166, v135
	ds_read2st64_b32 v[168:169], v151 offset0:112 offset1:116
	v_cvt_pk_fp8_f32 v166, v134, v137
	ds_read2st64_b32 v[170:171], v151 offset0:120 offset1:124
	v_med3_f32 v134, v167, s11, v155
	v_med3_f32 v137, v172, s11, v155
	v_cvt_pk_fp8_f32 v166, v134, v137 op_sel:[0,0,1]
	s_waitcnt lgkmcnt(1)
	v_mul_f32_e32 v134, 0x43000000, v168
	v_mul_f32_e32 v137, 0x43000000, v169
	s_waitcnt lgkmcnt(0)
	v_mul_f32_e32 v170, 0x43000000, v170
	v_med3_f32 v134, v134, s11, v155
	v_med3_f32 v137, v137, s11, v155
	v_mov_b32_e32 v167, v135
	ds_read2st64_b32 v[168:169], v151 offset0:128 offset1:132
	v_mul_f32_e32 v172, 0x43000000, v171
	v_cvt_pk_fp8_f32 v167, v134, v137
	v_med3_f32 v134, v170, s11, v155
	ds_read2st64_b32 v[170:171], v151 offset0:136 offset1:140
	v_med3_f32 v137, v172, s11, v155
	v_cvt_pk_fp8_f32 v167, v134, v137 op_sel:[0,0,1]
	s_waitcnt lgkmcnt(1)
	v_mul_f32_e32 v134, 0x43000000, v168
	v_mul_f32_e32 v137, 0x43000000, v169
	s_waitcnt lgkmcnt(0)
	v_mul_f32_e32 v169, 0x43000000, v170
	v_mul_f32_e32 v174, 0x43000000, v171
	v_med3_f32 v134, v134, s11, v155
	v_med3_f32 v137, v137, s11, v155
	v_mov_b32_e32 v168, v135
	ds_read2st64_b32 v[170:171], v151 offset0:144 offset1:148
	v_cvt_pk_fp8_f32 v168, v134, v137
	ds_read2st64_b32 v[172:173], v151 offset0:152 offset1:156
	v_med3_f32 v134, v169, s11, v155
	v_med3_f32 v137, v174, s11, v155
	v_cvt_pk_fp8_f32 v168, v134, v137 op_sel:[0,0,1]
	s_waitcnt lgkmcnt(1)
	v_mul_f32_e32 v134, 0x43000000, v170
	v_mul_f32_e32 v137, 0x43000000, v171
	s_waitcnt lgkmcnt(0)
	v_mul_f32_e32 v172, 0x43000000, v172
	v_med3_f32 v134, v134, s11, v155
	v_med3_f32 v137, v137, s11, v155
	v_mov_b32_e32 v169, v135
	ds_read2st64_b32 v[170:171], v151 offset0:160 offset1:164
	v_mul_f32_e32 v174, 0x43000000, v173
	v_cvt_pk_fp8_f32 v169, v134, v137
	v_med3_f32 v134, v172, s11, v155
	ds_read2st64_b32 v[172:173], v151 offset0:168 offset1:172
	v_med3_f32 v137, v174, s11, v155
	v_cvt_pk_fp8_f32 v169, v134, v137 op_sel:[0,0,1]
	s_waitcnt lgkmcnt(1)
	v_mul_f32_e32 v134, 0x43000000, v170
	v_mul_f32_e32 v137, 0x43000000, v171
	s_waitcnt lgkmcnt(0)
	v_mul_f32_e32 v171, 0x43000000, v172
	v_mul_f32_e32 v176, 0x43000000, v173
	v_med3_f32 v134, v134, s11, v155
	v_med3_f32 v137, v137, s11, v155
	v_mov_b32_e32 v170, v135
	ds_read2st64_b32 v[172:173], v151 offset0:176 offset1:180
	v_cvt_pk_fp8_f32 v170, v134, v137
	ds_read2st64_b32 v[174:175], v151 offset0:184 offset1:188
	v_med3_f32 v134, v171, s11, v155
	v_med3_f32 v137, v176, s11, v155
	v_cvt_pk_fp8_f32 v170, v134, v137 op_sel:[0,0,1]
	s_waitcnt lgkmcnt(1)
	v_mul_f32_e32 v134, 0x43000000, v172
	v_mul_f32_e32 v137, 0x43000000, v173
	s_waitcnt lgkmcnt(0)
	v_mul_f32_e32 v174, 0x43000000, v174
	v_med3_f32 v134, v134, s11, v155
	v_med3_f32 v137, v137, s11, v155
	v_mov_b32_e32 v171, v135
	ds_read2st64_b32 v[172:173], v151 offset0:192 offset1:196
	v_mul_f32_e32 v176, 0x43000000, v175
	v_cvt_pk_fp8_f32 v171, v134, v137
	v_med3_f32 v134, v174, s11, v155
	ds_read2st64_b32 v[174:175], v151 offset0:200 offset1:204
	v_med3_f32 v137, v176, s11, v155
	v_cvt_pk_fp8_f32 v171, v134, v137 op_sel:[0,0,1]
	s_waitcnt lgkmcnt(1)
	v_mul_f32_e32 v134, 0x43000000, v172
	v_mul_f32_e32 v137, 0x43000000, v173
	s_waitcnt lgkmcnt(0)
	v_mul_f32_e32 v173, 0x43000000, v174
	v_mul_f32_e32 v178, 0x43000000, v175
	v_med3_f32 v134, v134, s11, v155
	v_med3_f32 v137, v137, s11, v155
	v_mov_b32_e32 v172, v135
	ds_read2st64_b32 v[174:175], v151 offset0:208 offset1:212
	v_cvt_pk_fp8_f32 v172, v134, v137
	ds_read2st64_b32 v[176:177], v151 offset0:216 offset1:220
	v_med3_f32 v134, v173, s11, v155
	v_med3_f32 v137, v178, s11, v155
	v_cvt_pk_fp8_f32 v172, v134, v137 op_sel:[0,0,1]
	s_waitcnt lgkmcnt(1)
	v_mul_f32_e32 v134, 0x43000000, v174
	v_mul_f32_e32 v137, 0x43000000, v175
	s_waitcnt lgkmcnt(0)
	v_mul_f32_e32 v176, 0x43000000, v176
	v_med3_f32 v134, v134, s11, v155
	v_med3_f32 v137, v137, s11, v155
	v_mov_b32_e32 v173, v135
	ds_read2st64_b32 v[174:175], v151 offset0:224 offset1:228
	v_mul_f32_e32 v178, 0x43000000, v177
	v_cvt_pk_fp8_f32 v173, v134, v137
	v_med3_f32 v134, v176, s11, v155
	ds_read2st64_b32 v[176:177], v151 offset0:232 offset1:236
	v_med3_f32 v137, v178, s11, v155
	v_cvt_pk_fp8_f32 v173, v134, v137 op_sel:[0,0,1]
	s_waitcnt lgkmcnt(1)
	v_mul_f32_e32 v134, 0x43000000, v174
	v_mul_f32_e32 v137, 0x43000000, v175
	s_waitcnt lgkmcnt(0)
	v_mul_f32_e32 v175, 0x43000000, v176
	v_mul_f32_e32 v180, 0x43000000, v177
	v_med3_f32 v134, v134, s11, v155
	v_med3_f32 v137, v137, s11, v155
	v_mov_b32_e32 v174, v135
	ds_read2st64_b32 v[176:177], v151 offset0:240 offset1:244
	v_cvt_pk_fp8_f32 v174, v134, v137
	v_med3_f32 v134, v175, s11, v155
	ds_read2st64_b32 v[178:179], v151 offset0:248 offset1:252
	v_med3_f32 v137, v180, s11, v155
	v_cvt_pk_fp8_f32 v174, v134, v137 op_sel:[0,0,1]
	s_waitcnt lgkmcnt(1)
	v_mul_f32_e32 v134, 0x43000000, v176
	v_mul_f32_e32 v137, 0x43000000, v177
	v_med3_f32 v134, v134, s11, v155
	v_med3_f32 v137, v137, s11, v155
	v_mov_b32_e32 v175, v135
	v_cvt_pk_fp8_f32 v175, v134, v137
	s_waitcnt lgkmcnt(0)
	v_mul_f32_e32 v176, 0x43000000, v178
	v_mul_f32_e32 v134, 0x43000000, v179
	v_med3_f32 v137, v176, s11, v155
	v_med3_f32 v134, v134, s11, v155
	v_cvt_pk_fp8_f32 v175, v137, v134 op_sel:[0,0,1]
	s_barrier
	ds_write_b128 v156, v[130:133]
	ds_write_b128 v157, v[164:167]
	ds_write_b128 v158, v[168:171]
	ds_write_b128 v159, v[172:175]
	s_waitcnt lgkmcnt(0)
	s_barrier
	ds_read_b128 v[130:133], v160
	v_add_u32_e32 v164, s72, v140
	s_cselect_b64 s[44:45], -1, 0
	s_mov_b64 s[2:3], -1
	s_and_b64 vcc, exec, s[44:45]
	v_lshlrev_b32_e32 v165, 1, v164
	v_add_u32_e32 v137, s14, v138
	s_cbranch_vccz .Lcv_404
	v_lshlrev_b32_e32 v134, 2, v164
	v_lshrrev_b32_e32 v166, 1, v164
	v_and_b32_e32 v167, 0xffffffe3, v164
	v_and_or_b32 v168, v166, 12, v167
	v_and_or_b32 v169, v134, 16, v167
	v_ashrrev_i32_e32 v166, 7, v164
	v_ashrrev_i32_e32 v134, 7, v137
	v_mad_u64_u32 v[166:167], s[2:3], v166, 56, v[134:135]
	v_lshrrev_b32_e32 v134, 3, v169
	v_bfe_u32 v169, v137, 6, 1
	v_ashrrev_i32_e32 v167, 31, v166
	v_and_or_b32 v134, v134, 14, v169
	v_lshlrev_b32_e32 v168, 6, v168
	v_and_b32_e32 v169, 63, v137
	v_lshlrev_b64 v[166:167], 14, v[166:167]
	v_and_or_b32 v168, v168, s68, v169
	v_lshlrev_b32_e32 v134, 10, v134
	v_and_b32_e32 v169, 32, v165
	v_bitop3_b32 v134, v134, v168, v169 bitop3:0xf6
	v_lshl_add_u64 v[166:167], s[40:41], 0, v[166:167]
	v_lshl_add_u64 v[166:167], v[166:167], 0, v[134:135]
	s_waitcnt lgkmcnt(0)
	global_store_dwordx4 v[166:167], v[130:133], off nt
	s_mov_b64 s[2:3], 0
